# grid barrier: the XCD leader bumps its XCD generation word before (not after) its own acquire invalidate
# baseline (speedup 1.0000x reference)
.LBB0_163:
	s_or_b64 exec, exec, s[2:3]
	v_mov_b32_e32 v0, 0
	v_mov_b32_e32 v1, 1
	s_waitcnt vmcnt(0)
	global_atomic_add v0, v1, s[4:5]
	buffer_inv sc1
	s_waitcnt vmcnt(0)

.LBB0_353:
	s_or_b64 exec, exec, s[4:5]
	v_mov_b32_e32 v0, 0x2000
	v_mov_b32_e32 v1, 1
	s_waitcnt vmcnt(0)
	global_atomic_add v0, v1, s[2:3] offset:1024
	buffer_inv sc1
	s_waitcnt vmcnt(0)
